# baseline (speedup 1.0000x reference)
_Z11jacobi_mainPKfS0_S0_PyPf:
	s_lshl_b32 s3, s2, 3
	s_load_dwordx4 s[12:15], s[0:1], 0x0
	s_load_dwordx2 s[4:5], s[0:1], 0x10
	s_load_dwordx2 s[16:17], s[0:1], 0x20
	s_load_dwordx2 s[90:91], s[0:1], 0x18
	s_and_b32 s3, s3, 56
	s_ashr_i32 s33, s2, 5
	v_readfirstlane_b32 s40, v0
	s_add_i32 s18, s3, s33
	s_bfe_u32 s3, s2, 0x20003
	s_lshl_b32 s7, s3, 8
	s_and_b32 s10, s40, 0xffffffc0
	s_ashr_i32 s19, s18, 31
	s_lshr_b32 s34, s2, 3
	s_add_i32 s11, s10, s7
	s_lshl_b64 s[8:9], s[18:19], 22
	v_and_b32_e32 v206, 63, v0
	s_waitcnt lgkmcnt(0)
	s_add_u32 s8, s12, s8
	s_addc_u32 s9, s13, s9
	v_or_b32_e32 v154, s11, v206
	s_lshl_b32 s6, s18, 10
	v_add_u32_e32 v2, s6, v154
	v_ashrrev_i32_e32 v3, 31, v2
	v_lshlrev_b64 v[2:3], 2, v[2:3]
	v_lshl_add_u64 v[4:5], s[14:15], 0, v[2:3]
	global_load_dword v1, v[4:5], off
	s_movk_i32 s12, 0x1004
	v_mov_b64_e32 v[4:5], s[8:9]
	v_mad_i64_i32 v[4:5], s[12:13], v154, s12, v[4:5]
	v_lshl_add_u64 v[2:3], s[4:5], 0, v[2:3]
	global_load_dword v207, v[4:5], off
	global_load_dword v66, v[2:3], off
	s_lshl_b32 s76, s6, 2
	s_add_u32 s76, s4, s76
	s_addc_u32 s77, s5, 0
	v_lshlrev_b32_e32 v220, 4, v0
	global_load_dwordx4 v[224:227], v220, s[76:77]
	v_ashrrev_i32_e32 v155, 31, v154
	s_mov_b32 s21, 0
	s_lshr_b32 s35, s40, 6
	v_cmp_eq_u32_e64 s[12:13], 0, v206
	v_lshrrev_b32_e32 v67, 5, v206
	v_or_b32_e32 v132, s11, v67
	s_lshl_b64 s[14:15], s[18:19], 14
	v_ashrrev_i32_e32 v133, 31, v132
	v_and_b32_e32 v124, 31, v0
	s_waitcnt lgkmcnt(0)
	s_cmp_gt_u32 s40, 63
	s_cbranch_scc1 .Lpz_skip
	s_mul_i32 s94, s18, 0x650
	s_lshl_b32 s95, s3, 2
	s_add_u32 s94, s94, s95
	s_add_u32 s94, s16, s94
	s_addc_u32 s95, s17, 0
	v_lshlrev_b32_e32 v220, 4, v206
	v_mov_b32_e32 v221, 0
	global_store_dword v220, v221, s[94:95]
	v_cmp_gt_u32_e32 vcc, 36, v206
	s_and_saveexec_b64 s[92:93], vcc
	global_store_dword v220, v221, s[94:95] offset:1024
	s_mov_b64 exec, s[92:93]
.Lpz_skip:
	s_add_u32 s14, s90, s14
	v_lshlrev_b64 v[2:3], 12, v[132:133]
	s_addc_u32 s15, s91, s15
	s_add_i32 s0, s7, 0x100
	v_lshl_add_u64 v[2:3], s[8:9], 0, v[2:3]
	v_lshlrev_b32_e32 v190, 4, v124
	v_mov_b32_e32 v191, 0
	s_and_b32 s26, s0, 0x300
	v_lshl_add_u64 v[130:131], v[2:3], 0, v[190:191]
	s_mov_b64 s[0:1], 0x30000
	v_lshl_add_u64 v[126:127], v[130:131], 0, s[0:1]
	s_mov_b64 s[0:1], 0x32000
	v_lshl_add_u64 v[128:129], v[130:131], 0, s[0:1]
	s_mov_b64 s[0:1], 0x34000
	v_lshl_add_u64 v[134:135], v[130:131], 0, s[0:1]
	s_mov_b64 s[0:1], 0x36000
	v_lshl_add_u64 v[136:137], v[130:131], 0, s[0:1]
	s_mov_b64 s[0:1], 0x38000
	v_lshl_add_u64 v[138:139], v[130:131], 0, s[0:1]
	s_mov_b64 s[0:1], 0x3a000
	v_lshl_add_u64 v[140:141], v[130:131], 0, s[0:1]
	s_mov_b64 s[0:1], 0x3c000
	s_or_b32 s24, s7, 0x80
	v_lshl_add_u64 v[142:143], v[130:131], 0, s[0:1]
	s_mov_b64 s[0:1], 0x3e000
	s_lshl_b32 s20, s7, 2
	v_lshl_add_u64 v[144:145], v[130:131], 0, s[0:1]
	s_lshl_b32 s8, s24, 2
	s_mov_b32 s9, s21
	v_lshl_add_u64 v[2:3], v[126:127], 0, s[20:21]
	v_lshl_add_u64 v[4:5], v[128:129], 0, s[20:21]
	v_lshl_add_u64 v[6:7], v[134:135], 0, s[20:21]
	v_lshl_add_u64 v[8:9], v[136:137], 0, s[20:21]
	v_lshl_add_u64 v[10:11], v[138:139], 0, s[20:21]
	v_lshl_add_u64 v[12:13], v[140:141], 0, s[20:21]
	v_lshl_add_u64 v[14:15], v[142:143], 0, s[20:21]
	v_lshl_add_u64 v[16:17], v[144:145], 0, s[20:21]
	v_lshl_add_u64 v[18:19], v[126:127], 0, s[8:9]
	v_lshl_add_u64 v[20:21], v[128:129], 0, s[8:9]
	v_lshl_add_u64 v[22:23], v[134:135], 0, s[8:9]
	v_lshl_add_u64 v[24:25], v[136:137], 0, s[8:9]
	s_lshl_b32 s0, s26, 2
	s_mov_b32 s1, s21
	v_lshl_add_u64 v[72:73], v[138:139], 0, s[8:9]
	v_lshl_add_u64 v[102:103], v[140:141], 0, s[8:9]
	v_lshl_add_u64 v[104:105], v[142:143], 0, s[8:9]
	v_lshl_add_u64 v[106:107], v[144:145], 0, s[8:9]
	v_lshl_add_u64 v[108:109], v[126:127], 0, s[0:1]
	v_lshl_add_u64 v[110:111], v[128:129], 0, s[0:1]
	v_lshl_add_u64 v[112:113], v[134:135], 0, s[0:1]
	v_lshl_add_u64 v[114:115], v[136:137], 0, s[0:1]
	v_lshl_add_u64 v[116:117], v[138:139], 0, s[0:1]
	v_lshl_add_u64 v[118:119], v[140:141], 0, s[0:1]
	v_lshl_add_u64 v[120:121], v[142:143], 0, s[0:1]
	v_lshl_add_u64 v[122:123], v[144:145], 0, s[0:1]
	global_load_dwordx4 v[68:71], v[2:3], off nt
	global_load_dwordx4 v[78:81], v[4:5], off nt
	global_load_dwordx4 v[82:85], v[6:7], off nt
	global_load_dwordx4 v[90:93], v[8:9], off nt
	global_load_dwordx4 v[98:101], v[10:11], off nt
	global_load_dwordx4 v[62:65], v[12:13], off nt
	global_load_dwordx4 v[54:57], v[14:15], off nt
	global_load_dwordx4 v[46:49], v[16:17], off nt
	global_load_dwordx4 v[94:97], v[18:19], off nt
	global_load_dwordx4 v[86:89], v[20:21], off nt
	global_load_dwordx4 v[74:77], v[22:23], off nt
	global_load_dwordx4 v[58:61], v[24:25], off nt
	global_load_dwordx4 v[50:53], v[72:73], off nt
	global_load_dwordx4 v[42:45], v[102:103], off nt
	global_load_dwordx4 v[38:41], v[104:105], off nt
	global_load_dwordx4 v[34:37], v[106:107], off nt
	global_load_dwordx4 v[30:33], v[108:109], off nt
	global_load_dwordx4 v[26:29], v[110:111], off nt
	s_nop 0
	global_load_dwordx4 v[22:25], v[112:113], off nt
	global_load_dwordx4 v[18:21], v[114:115], off nt
	global_load_dwordx4 v[14:17], v[116:117], off nt
	global_load_dwordx4 v[10:13], v[118:119], off nt
	global_load_dwordx4 v[6:9], v[120:121], off nt
	global_load_dwordx4 v[2:5], v[122:123], off nt
	s_waitcnt vmcnt(25)
	v_div_scale_f32 v72, s[22:23], v207, v207, 1.0
	v_rcp_f32_e32 v73, v72
	s_lshl_b32 s11, s10, 2
	s_mul_i32 s19, s35, 0x1100
	s_add_i32 s22, s11, 0x26600
	v_fma_f32 v103, -v72, v73, 1.0
	v_fmac_f32_e32 v73, v103, v73
	v_div_scale_f32 v103, vcc, 1.0, v207, 1.0
	v_mul_f32_e32 v104, v103, v73
	v_fma_f32 v105, -v72, v104, v103
	v_fmac_f32_e32 v104, v105, v73
	v_fma_f32 v72, -v72, v104, v103
	v_div_fmas_f32 v72, v72, v73, v104
	v_div_fixup_f32 v72, v72, v207, 1.0
	s_waitcnt vmcnt(24)
	v_fma_f32 v208, v72, v1, -v66
	v_mbcnt_lo_u32_b32 v244, -1, 0
	v_mbcnt_hi_u32_b32 v244, -1, v244
	v_and_b32_e32 v245, 64, v244
	v_xor_b32_e32 v246, 32, v244
	v_add_u32_e32 v245, 64, v245
	v_cmp_lt_i32_e32 vcc, v246, v245
	v_xor_b32_e32 v248, 8, v244
	s_nop 0
	v_cndmask_b32_e32 v246, v244, v246, vcc
	v_lshlrev_b32_e32 v246, 2, v246
	v_mul_f32_e32 v247, v1, v1
	ds_bpermute_b32 v246, v246, v247
	v_xor_b32_e32 v247, 16, v244
	v_cmp_lt_i32_e32 vcc, v247, v245
	s_waitcnt lgkmcnt(0)
	v_fmac_f32_e32 v246, v1, v1
	v_cndmask_b32_e32 v247, v244, v247, vcc
	v_lshlrev_b32_e32 v247, 2, v247
	ds_bpermute_b32 v247, v247, v246
	v_cmp_lt_i32_e32 vcc, v248, v245
	s_waitcnt lgkmcnt(0)
	v_add_f32_e32 v246, v246, v247
	v_cndmask_b32_e32 v248, v244, v248, vcc
	v_lshlrev_b32_e32 v248, 2, v248
	ds_bpermute_b32 v247, v248, v246
	v_xor_b32_e32 v248, 4, v244
	v_cmp_lt_i32_e32 vcc, v248, v245
	s_waitcnt lgkmcnt(0)
	v_add_f32_e32 v246, v246, v247
	v_cndmask_b32_e32 v248, v244, v248, vcc
	v_lshlrev_b32_e32 v248, 2, v248
	ds_bpermute_b32 v247, v248, v246
	v_xor_b32_e32 v248, 2, v244
	v_cmp_lt_i32_e32 vcc, v248, v245
	s_waitcnt lgkmcnt(0)
	v_add_f32_e32 v246, v246, v247
	v_cndmask_b32_e32 v248, v244, v248, vcc
	v_lshlrev_b32_e32 v248, 2, v248
	ds_bpermute_b32 v247, v248, v246
	v_xor_b32_e32 v248, 1, v244
	v_cmp_lt_i32_e32 vcc, v248, v245
	s_nop 1
	v_cndmask_b32_e32 v245, v244, v248, vcc
	s_waitcnt lgkmcnt(0)
	v_add_f32_e32 v244, v246, v247
	v_lshlrev_b32_e32 v245, 2, v245
	ds_bpermute_b32 v245, v245, v244
	s_and_saveexec_b64 s[80:81], s[12:13]
	s_cbranch_execz .LBB0_2
	s_lshl_b32 s82, s35, 2
	s_add_i32 s82, s82, 0x26a00
	s_waitcnt lgkmcnt(0)
	v_add_f32_e32 v244, v244, v245
	v_mov_b32_e32 v245, s82
	ds_write_b32 v245, v244
